# baseline (speedup 1.0000x reference)
.Lmy_s2_nodma3:
	ds_read_b128 v[160:163], v213 offset:16384
	ds_read_b128 v[164:167], v213 offset:20480
	ds_read_b128 v[168:171], v213 offset:24576
	ds_read_b128 v[172:175], v213 offset:28672
	s_waitcnt lgkmcnt(4)
	v_mfma_f32_16x16x32_f16 v[96:99], v[144:147], v[44:47], 0
	v_mfma_f32_16x16x32_f16 v[100:103], v[148:151], v[44:47], 0
	v_mfma_f32_16x16x32_f16 v[104:107], v[152:155], v[44:47], 0
	v_mfma_f32_16x16x32_f16 v[108:111], v[156:159], v[44:47], 0
	ds_read_b128 v[144:147], v214 offset:16384
	ds_read_b128 v[148:151], v214 offset:20480
	ds_read_b128 v[152:155], v214 offset:24576
	ds_read_b128 v[156:159], v214 offset:28672
	s_waitcnt lgkmcnt(4)
	v_mfma_f32_16x16x32_f16 v[96:99], v[160:163], v[48:51], v[96:99]
	v_mfma_f32_16x16x32_f16 v[100:103], v[164:167], v[48:51], v[100:103]
	v_mfma_f32_16x16x32_f16 v[104:107], v[168:171], v[48:51], v[104:107]
	v_mfma_f32_16x16x32_f16 v[108:111], v[172:175], v[48:51], v[108:111]
	ds_read_b128 v[160:163], v215 offset:16384
	ds_read_b128 v[164:167], v215 offset:20480
	ds_read_b128 v[168:171], v215 offset:24576
	ds_read_b128 v[172:175], v215 offset:28672
	s_waitcnt lgkmcnt(4)
	v_mfma_f32_16x16x32_f16 v[96:99], v[144:147], v[52:55], v[96:99]
	v_mfma_f32_16x16x32_f16 v[100:103], v[148:151], v[52:55], v[100:103]
	v_mfma_f32_16x16x32_f16 v[104:107], v[152:155], v[52:55], v[104:107]
	v_mfma_f32_16x16x32_f16 v[108:111], v[156:159], v[52:55], v[108:111]
	ds_read_b128 v[176:179], v221 offset:49664
	ds_read_b128 v[180:183], v221 offset:49680
	ds_read_b32 v188, v221 offset:49152
	ds_read_b128 v[144:147], v212 offset:0
	ds_read_b128 v[148:151], v212 offset:4096
	ds_read_b128 v[152:155], v212 offset:8192
	ds_read_b128 v[156:159], v212 offset:12288
	s_waitcnt lgkmcnt(7)
	v_mfma_f32_16x16x32_f16 v[96:99], v[160:163], v[56:59], v[96:99]
	v_mfma_f32_16x16x32_f16 v[100:103], v[164:167], v[56:59], v[100:103]
	v_mfma_f32_16x16x32_f16 v[104:107], v[168:171], v[56:59], v[104:107]
	v_mfma_f32_16x16x32_f16 v[108:111], v[172:175], v[56:59], v[108:111]
	v_mul_f32_e32 v189, 0x3fb8aa3b, v189
	ds_read_b64 v[234:235], v216 offset:32768
	ds_read_b64 v[236:237], v217 offset:32768
	ds_read_b64 v[238:239], v218 offset:32768
	ds_read_b64 v[240:241], v219 offset:32768
	ds_read_b128 v[224:227], v221 offset:49792
	ds_read_b128 v[228:231], v221 offset:49808
	ds_read_b32 v232, v221 offset:49280
	ds_read_b128 v[160:163], v213 offset:0
	ds_read_b128 v[164:167], v213 offset:4096
	ds_read_b128 v[168:171], v213 offset:8192
	ds_read_b128 v[172:175], v213 offset:12288
	s_waitcnt lgkmcnt(11)
	v_fma_f32 v188, v188, s51, v189
	v_exp_f32_e32 v188, v188
	s_cmp_eq_u32 s42, 0
	v_pk_mul_f32 v[176:177], v[176:177], v[188:189] op_sel_hi:[1,0]
	v_pk_mul_f32 v[178:179], v[178:179], v[188:189] op_sel_hi:[1,0]
	v_pk_mul_f32 v[180:181], v[180:181], v[188:189] op_sel_hi:[1,0]
	v_pk_mul_f32 v[182:183], v[182:183], v[188:189] op_sel_hi:[1,0]
	v_pk_mul_f32 v[176:177], v[60:61], v[176:177]
	v_pk_mul_f32 v[178:179], v[62:63], v[178:179]
	v_pk_mul_f32 v[180:181], v[64:65], v[180:181]
	v_pk_mul_f32 v[182:183], v[66:67], v[182:183]
	s_cbranch_scc0 .Lmy_s2_nomask5
	v_cndmask_b32_e64 v176, 0, v176, s[52:53]
	v_cndmask_b32_e64 v177, 0, v177, s[54:55]
	v_cndmask_b32_e64 v178, 0, v178, s[56:57]
	v_cndmask_b32_e64 v179, 0, v179, s[58:59]
	v_cndmask_b32_e64 v180, 0, v180, s[60:61]
	v_cndmask_b32_e64 v181, 0, v181, s[62:63]
	v_cndmask_b32_e64 v182, 0, v182, s[64:65]
	v_cndmask_b32_e64 v183, 0, v183, s[66:67]
.Lmy_s2_nomask5:
	v_cvt_pk_f16_f32 v184, v176, v177
	v_cvt_pk_f16_f32 v185, v178, v179
	v_cvt_pk_f16_f32 v186, v180, v181
	v_cvt_pk_f16_f32 v187, v182, v183
	s_nop 1
	v_mfma_f32_16x16x32_f16 v[112:115], v[144:147], v[184:187], 0
	v_mfma_f32_16x16x32_f16 v[116:119], v[148:151], v[184:187], 0
	v_mfma_f32_16x16x32_f16 v[120:123], v[152:155], v[184:187], 0
	v_mfma_f32_16x16x32_f16 v[124:127], v[156:159], v[184:187], 0
	s_cbranch_scc0 .Lmy_s2_nodiag6
	v_mfma_f32_16x16x32_f16 v[128:131], v[144:147], v[92:95], 0
	v_mfma_f32_16x16x32_f16 v[132:135], v[148:151], v[92:95], 0
	v_mfma_f32_16x16x32_f16 v[136:139], v[152:155], v[92:95], 0
	v_mfma_f32_16x16x32_f16 v[140:143], v[156:159], v[92:95], 0
	s_branch .Lmy_s2_kend4
.Lmy_s2_nodiag6:
	ds_read_b128 v[176:179], v221 offset:49920
	ds_read_b128 v[180:183], v221 offset:49936
	ds_read_b32 v188, v221 offset:49408
	ds_read_b128 v[144:147], v214 offset:0
	ds_read_b128 v[148:151], v214 offset:4096
	ds_read_b128 v[152:155], v214 offset:8192
	ds_read_b128 v[156:159], v214 offset:12288
	s_waitcnt lgkmcnt(7)
	v_fma_f32 v232, v232, s51, v189
	v_exp_f32_e32 v232, v232
	s_cmp_eq_u32 s42, 1
	v_pk_mul_f32 v[224:225], v[224:225], v[232:233] op_sel_hi:[1,0]
	v_pk_mul_f32 v[226:227], v[226:227], v[232:233] op_sel_hi:[1,0]
	v_pk_mul_f32 v[228:229], v[228:229], v[232:233] op_sel_hi:[1,0]
	v_pk_mul_f32 v[230:231], v[230:231], v[232:233] op_sel_hi:[1,0]
	v_pk_mul_f32 v[224:225], v[68:69], v[224:225]
	v_pk_mul_f32 v[226:227], v[70:71], v[226:227]
	v_pk_mul_f32 v[228:229], v[72:73], v[228:229]
	v_pk_mul_f32 v[230:231], v[74:75], v[230:231]
	s_cbranch_scc0 .Lmy_s2_nomask7
	v_cndmask_b32_e64 v224, 0, v224, s[52:53]
	v_cndmask_b32_e64 v225, 0, v225, s[54:55]
	v_cndmask_b32_e64 v226, 0, v226, s[56:57]
	v_cndmask_b32_e64 v227, 0, v227, s[58:59]
	v_cndmask_b32_e64 v228, 0, v228, s[60:61]
	v_cndmask_b32_e64 v229, 0, v229, s[62:63]
	v_cndmask_b32_e64 v230, 0, v230, s[64:65]
	v_cndmask_b32_e64 v231, 0, v231, s[66:67]
.Lmy_s2_nomask7:
	v_cvt_pk_f16_f32 v184, v224, v225
	v_cvt_pk_f16_f32 v185, v226, v227
	v_cvt_pk_f16_f32 v186, v228, v229
	v_cvt_pk_f16_f32 v187, v230, v231
	s_nop 1
	v_mfma_f32_16x16x32_f16 v[112:115], v[160:163], v[184:187], v[112:115]
	v_mfma_f32_16x16x32_f16 v[116:119], v[164:167], v[184:187], v[116:119]
	v_mfma_f32_16x16x32_f16 v[120:123], v[168:171], v[184:187], v[120:123]
	v_mfma_f32_16x16x32_f16 v[124:127], v[172:175], v[184:187], v[124:127]
	s_cbranch_scc0 .Lmy_s2_nodiag8
	v_mfma_f32_16x16x32_f16 v[128:131], v[160:163], v[92:95], 0
	v_mfma_f32_16x16x32_f16 v[132:135], v[164:167], v[92:95], 0
	v_mfma_f32_16x16x32_f16 v[136:139], v[168:171], v[92:95], 0
	v_mfma_f32_16x16x32_f16 v[140:143], v[172:175], v[92:95], 0
	s_branch .Lmy_s2_kend4
.Lmy_s2_nodiag8:
	ds_read_b128 v[224:227], v221 offset:50048
	ds_read_b128 v[228:231], v221 offset:50064
	ds_read_b32 v232, v221 offset:49536
	ds_read_b128 v[160:163], v215 offset:0
	ds_read_b128 v[164:167], v215 offset:4096
	ds_read_b128 v[168:171], v215 offset:8192
	ds_read_b128 v[172:175], v215 offset:12288
	s_waitcnt lgkmcnt(7)
	v_fma_f32 v188, v188, s51, v189
	v_exp_f32_e32 v188, v188
	s_cmp_eq_u32 s42, 2
	v_pk_mul_f32 v[176:177], v[176:177], v[188:189] op_sel_hi:[1,0]
	v_pk_mul_f32 v[178:179], v[178:179], v[188:189] op_sel_hi:[1,0]
	v_pk_mul_f32 v[180:181], v[180:181], v[188:189] op_sel_hi:[1,0]
	v_pk_mul_f32 v[182:183], v[182:183], v[188:189] op_sel_hi:[1,0]
	v_pk_mul_f32 v[176:177], v[76:77], v[176:177]
	v_pk_mul_f32 v[178:179], v[78:79], v[178:179]
	v_pk_mul_f32 v[180:181], v[80:81], v[180:181]
	v_pk_mul_f32 v[182:183], v[82:83], v[182:183]
	s_cbranch_scc0 .Lmy_s2_nomask9
	v_cndmask_b32_e64 v176, 0, v176, s[52:53]
	v_cndmask_b32_e64 v177, 0, v177, s[54:55]
	v_cndmask_b32_e64 v178, 0, v178, s[56:57]
	v_cndmask_b32_e64 v179, 0, v179, s[58:59]
	v_cndmask_b32_e64 v180, 0, v180, s[60:61]
	v_cndmask_b32_e64 v181, 0, v181, s[62:63]
	v_cndmask_b32_e64 v182, 0, v182, s[64:65]
	v_cndmask_b32_e64 v183, 0, v183, s[66:67]
.Lmy_s2_nomask9:
	v_cvt_pk_f16_f32 v184, v176, v177
	v_cvt_pk_f16_f32 v185, v178, v179
	v_cvt_pk_f16_f32 v186, v180, v181
	v_cvt_pk_f16_f32 v187, v182, v183
	s_nop 1
	v_mfma_f32_16x16x32_f16 v[112:115], v[144:147], v[184:187], v[112:115]
	v_mfma_f32_16x16x32_f16 v[116:119], v[148:151], v[184:187], v[116:119]
	v_mfma_f32_16x16x32_f16 v[120:123], v[152:155], v[184:187], v[120:123]
	v_mfma_f32_16x16x32_f16 v[124:127], v[156:159], v[184:187], v[124:127]
	s_cbranch_scc0 .Lmy_s2_nodiag10
	v_mfma_f32_16x16x32_f16 v[128:131], v[144:147], v[92:95], 0
	v_mfma_f32_16x16x32_f16 v[132:135], v[148:151], v[92:95], 0
	v_mfma_f32_16x16x32_f16 v[136:139], v[152:155], v[92:95], 0
	v_mfma_f32_16x16x32_f16 v[140:143], v[156:159], v[92:95], 0
	s_branch .Lmy_s2_kend4
.Lmy_s2_nodiag10:
	s_waitcnt lgkmcnt(0)
	v_fma_f32 v232, v232, s51, v189
	v_exp_f32_e32 v232, v232
	s_cmp_eq_u32 s42, 3
	v_pk_mul_f32 v[224:225], v[224:225], v[232:233] op_sel_hi:[1,0]
	v_pk_mul_f32 v[226:227], v[226:227], v[232:233] op_sel_hi:[1,0]
	v_pk_mul_f32 v[228:229], v[228:229], v[232:233] op_sel_hi:[1,0]
	v_pk_mul_f32 v[230:231], v[230:231], v[232:233] op_sel_hi:[1,0]
	v_pk_mul_f32 v[224:225], v[84:85], v[224:225]
	v_pk_mul_f32 v[226:227], v[86:87], v[226:227]
	v_pk_mul_f32 v[228:229], v[88:89], v[228:229]
	v_pk_mul_f32 v[230:231], v[90:91], v[230:231]
	s_cbranch_scc0 .Lmy_s2_nomask11
	v_cndmask_b32_e64 v224, 0, v224, s[52:53]
	v_cndmask_b32_e64 v225, 0, v225, s[54:55]
	v_cndmask_b32_e64 v226, 0, v226, s[56:57]
	v_cndmask_b32_e64 v227, 0, v227, s[58:59]
	v_cndmask_b32_e64 v228, 0, v228, s[60:61]
	v_cndmask_b32_e64 v229, 0, v229, s[62:63]
	v_cndmask_b32_e64 v230, 0, v230, s[64:65]
	v_cndmask_b32_e64 v231, 0, v231, s[66:67]
.Lmy_s2_nomask11:
	v_cvt_pk_f16_f32 v184, v224, v225
	v_cvt_pk_f16_f32 v185, v226, v227
	v_cvt_pk_f16_f32 v186, v228, v229
	v_cvt_pk_f16_f32 v187, v230, v231
	s_nop 1
	v_mfma_f32_16x16x32_f16 v[112:115], v[160:163], v[184:187], v[112:115]
	v_mfma_f32_16x16x32_f16 v[116:119], v[164:167], v[184:187], v[116:119]
	v_mfma_f32_16x16x32_f16 v[120:123], v[168:171], v[184:187], v[120:123]
	v_mfma_f32_16x16x32_f16 v[124:127], v[172:175], v[184:187], v[124:127]
	v_mfma_f32_16x16x32_f16 v[128:131], v[160:163], v[92:95], 0
	v_mfma_f32_16x16x32_f16 v[132:135], v[164:167], v[92:95], 0
	v_mfma_f32_16x16x32_f16 v[136:139], v[168:171], v[92:95], 0
	v_mfma_f32_16x16x32_f16 v[140:143], v[172:175], v[92:95], 0
